# retention in-projection epilogue (rotary tiles): all eight cos/sin table load pairs issued in the first row block into spare VGPRs; per-block waits (which also drained the previous block's stores) rem
# speedup vs baseline: 1.0036x; 1.0000x over previous
; #define GAS __attribute__((address_space(1)))
;     __device__ __forceinline__ void operator()(const f32x4 (&acc)[2][2][4][2], const Unit& u, int wr, int wc, int fr, int fq) const {
;     ...
;                 const int row = row0 + ai * HALF + m * 16; bf16_t* rowp = base + (size_t)row * ld + col0;
;                 f32x4 v00 = acc[ai][0][m][0], v01 = acc[ai][0][m][1], v10 = acc[ai][1][m][0], v11 = acc[ai][1][m][1];
;                 if (do_rope) {
;                     const GAS u32x4* rp = (const GAS u32x4*)(rope + (size_t)row * 128 + wc * 32 + 8 * fq);
;                     const u32x4 ta = rp[0], tb = rp[1];
;                     { f32x4 a, b;
;                       a[0] = v00[0] * bf_lo(ta.x) - v10[0] * bf_hi(ta.x); b[0] = v10[0] * bf_lo(ta.x) + v00[0] * bf_hi(ta.x);
;                       a[1] = v00[1] * bf_lo(ta.y) - v10[1] * bf_hi(ta.y); b[1] = v10[1] * bf_lo(ta.y) + v00[1] * bf_hi(ta.y);
;                       a[2] = v00[2] * bf_lo(ta.z) - v10[2] * bf_hi(ta.z); b[2] = v10[2] * bf_lo(ta.z) + v00[2] * bf_hi(ta.z);
;                       a[3] = v00[3] * bf_lo(ta.w) - v10[3] * bf_hi(ta.w); b[3] = v10[3] * bf_lo(ta.w) + v00[3] * bf_hi(ta.w);
;                       v00 = a; v10 = b; }
;                     FENCE();
;                     { f32x4 a, b;
;                       a[0] = v01[0] * bf_lo(tb.x) - v11[0] * bf_hi(tb.x); b[0] = v11[0] * bf_lo(tb.x) + v01[0] * bf_hi(tb.x);
;                       a[1] = v01[1] * bf_lo(tb.y) - v11[1] * bf_hi(tb.y); b[1] = v11[1] * bf_lo(tb.y) + v01[1] * bf_hi(tb.y);
;                       a[2] = v01[2] * bf_lo(tb.z) - v11[2] * bf_hi(tb.z); b[2] = v11[2] * bf_lo(tb.z) + v01[2] * bf_hi(tb.z);
;                       a[3] = v01[3] * bf_lo(tb.w) - v11[3] * bf_hi(tb.w); b[3] = v11[3] * bf_lo(tb.w) + v01[3] * bf_hi(tb.w);
;                       v01 = a; v11 = b; }
;                 }
;                 v00 = v00 * sc; v01 = v01 * sc; v10 = v10 * sc; v11 = v11 * sc;
;                 u32x4 w0, w1;
;                 w0.x = cvt_pk_bf16(v00[0], v00[1]); w0.y = cvt_pk_bf16(v00[2], v00[3]); w0.z = cvt_pk_bf16(v01[0], v01[1]); w0.w = cvt_pk_bf16(v01[2], v01[3]);
;                 w1.x = cvt_pk_bf16(v10[0], v10[1]); w1.y = cvt_pk_bf16(v10[2], v10[3]); w1.z = cvt_pk_bf16(v11[0], v11[1]); w1.w = cvt_pk_bf16(v11[2], v11[3]);
;                 *(u32x4*)(rowp) = w0; *(u32x4*)(rowp + HALF) = w1;
.LBB0_1677:
	s_cmp_lt_i32 s78, 8
	s_cselect_b64 s[40:41], -1, 0
	s_cmp_gt_i32 s78, 7
	v_ashrrev_i32_e32 v135, 31, v134
	v_lshlrev_b32_e32 v132, 2, v138
	s_cbranch_scc1 .LBB0_1679
	v_lshlrev_b64 v[128:129], 9, v[134:135]
	v_lshl_add_u64 v[128:129], s[20:21], 0, v[128:129]
	v_lshl_add_u64 v[136:137], v[128:129], 0, v[132:133]
	global_load_dwordx4 v[128:131], v[136:137], off
	global_load_dwordx4 v[154:157], v[136:137], off offset:16
	v_mov_b32_e32 v224, 0x2000
	v_mov_b32_e32 v225, 0
	v_mov_b32_e32 v226, 0x10000
	v_mov_b32_e32 v227, 0
	v_lshl_add_u64 v[222:223], v[136:137], 0, v[224:225]
	global_load_dwordx4 v[166:169], v[222:223], off
	global_load_dwordx4 v[170:173], v[222:223], off offset:16
	v_lshl_add_u64 v[222:223], v[222:223], 0, v[224:225]
	global_load_dwordx4 v[174:177], v[222:223], off
	global_load_dwordx4 v[178:181], v[222:223], off offset:16
	v_lshl_add_u64 v[222:223], v[222:223], 0, v[224:225]
	global_load_dwordx4 v[182:185], v[222:223], off
	global_load_dwordx4 v[186:189], v[222:223], off offset:16
	v_lshl_add_u64 v[222:223], v[136:137], 0, v[226:227]
	global_load_dwordx4 v[190:193], v[222:223], off
	global_load_dwordx4 v[194:197], v[222:223], off offset:16
	v_lshl_add_u64 v[222:223], v[222:223], 0, v[224:225]
	global_load_dwordx4 v[198:201], v[222:223], off
	global_load_dwordx4 v[202:205], v[222:223], off offset:16
	v_lshl_add_u64 v[222:223], v[222:223], 0, v[224:225]
	global_load_dwordx4 v[206:209], v[222:223], off
	global_load_dwordx4 v[210:213], v[222:223], off offset:16
	v_lshl_add_u64 v[222:223], v[222:223], 0, v[224:225]
	global_load_dwordx4 v[214:217], v[222:223], off
	global_load_dwordx4 v[218:221], v[222:223], off offset:16
	s_waitcnt vmcnt(1)
	v_lshlrev_b32_e32 v135, 16, v130
	v_and_b32_e32 v139, 0xffff0000, v130
	v_lshlrev_b32_e32 v130, 16, v131
	v_and_b32_e32 v131, 0xffff0000, v131
	v_mul_f32_e32 v158, v126, v135
	v_mul_f32_e32 v160, v118, v139
	v_mul_f32_e32 v162, v118, v135
	v_mul_f32_e32 v164, v126, v139
	v_mov_b32_e32 v118, v127
	v_mov_b32_e32 v126, v119
	v_lshlrev_b32_e32 v137, 16, v129
	v_lshlrev_b32_e32 v136, 16, v128
	v_and_b32_e32 v129, 0xffff0000, v129
	v_and_b32_e32 v128, 0xffff0000, v128
	v_pk_mul_f32 v[118:119], v[118:119], v[130:131]
	v_pk_mul_f32 v[126:127], v[126:127], v[130:131]
	v_pk_mul_f32 v[140:141], v[124:125], v[128:129]
	v_pk_mul_f32 v[128:129], v[116:117], v[128:129]
	v_mov_b32_e32 v159, v118
	v_mov_b32_e32 v161, v119
	v_mov_b32_e32 v163, v126
	v_mov_b32_e32 v165, v127
	v_pk_fma_f32 v[124:125], v[124:125], v[136:137], v[128:129] neg_lo:[0,0,1] neg_hi:[0,0,1]
	v_pk_fma_f32 v[116:117], v[116:117], v[136:137], v[140:141]
	v_pk_add_f32 v[126:127], v[158:159], v[160:161] neg_lo:[0,1] neg_hi:[0,1]
	v_pk_add_f32 v[118:119], v[162:163], v[164:165]
	s_waitcnt vmcnt(0)
	v_lshlrev_b32_e32 v135, 16, v156
	v_and_b32_e32 v139, 0xffff0000, v156
	v_lshlrev_b32_e32 v128, 16, v154
	v_and_b32_e32 v130, 0xffff0000, v154
	v_mul_f32_e32 v154, v114, v139
	v_mul_f32_e32 v156, v114, v135
	v_lshlrev_b32_e32 v160, 16, v157
	v_and_b32_e32 v161, 0xffff0000, v157
	v_mov_b32_e32 v114, v123
	v_and_b32_e32 v131, 0xffff0000, v155
	v_mul_f32_e32 v140, v122, v135
	v_mul_f32_e32 v158, v122, v139
	v_pk_mul_f32 v[162:163], v[114:115], v[160:161]
	v_mov_b32_e32 v122, v115
	v_lshlrev_b32_e32 v129, 16, v155
	v_pk_mul_f32 v[136:137], v[120:121], v[130:131]
	v_pk_mul_f32 v[130:131], v[112:113], v[130:131]
	v_mov_b32_e32 v141, v162
	v_mov_b32_e32 v155, v163
	v_pk_mul_f32 v[114:115], v[122:123], v[160:161]
	v_pk_fma_f32 v[120:121], v[120:121], v[128:129], v[130:131] neg_lo:[0,0,1] neg_hi:[0,0,1]
	v_pk_add_f32 v[130:131], v[140:141], v[154:155] neg_lo:[0,1] neg_hi:[0,1]
	v_mov_b32_e32 v157, v114
	v_mov_b32_e32 v159, v115
	v_pk_fma_f32 v[112:113], v[112:113], v[128:129], v[136:137]
	v_pk_add_f32 v[114:115], v[156:157], v[158:159]
	v_mov_b32_e32 v122, v130
	v_mov_b32_e32 v123, v131
.LBB0_1679:
	s_lshl_b32 s4, s78, 8
	s_or_b32 s4, s4, s14
	s_cmp_lt_i32 s78, 4
	v_or_b32_e32 v128, s4, v138
	s_cselect_b64 vcc, -1, 0
	v_mov_b32_e32 v129, 0x3a000000
	v_bfrev_b32_e32 v130, 28
	v_cndmask_b32_e32 v136, v129, v130, vcc
	v_ashrrev_i32_e32 v129, 31, v128
	v_lshl_add_u64 v[138:139], v[128:129], 1, s[10:11]
	v_mad_i64_i32 v[128:129], s[4:5], v134, s76, v[138:139]
	v_pk_mul_f32 v[126:127], v[136:137], v[126:127] op_sel_hi:[0,1]
	v_pk_mul_f32 v[124:125], v[136:137], v[124:125] op_sel_hi:[0,1]
	v_pk_mul_f32 v[122:123], v[136:137], v[122:123] op_sel_hi:[0,1]
	v_pk_mul_f32 v[120:121], v[136:137], v[120:121] op_sel_hi:[0,1]
	v_pk_mul_f32 v[118:119], v[136:137], v[118:119] op_sel_hi:[0,1]
	v_pk_mul_f32 v[116:117], v[136:137], v[116:117] op_sel_hi:[0,1]
	v_pk_mul_f32 v[130:131], v[136:137], v[114:115] op_sel_hi:[0,1]
	v_pk_mul_f32 v[140:141], v[136:137], v[112:113] op_sel_hi:[0,1]
	v_cvt_pk_bf16_f32 v112, v124, v125
	v_cvt_pk_bf16_f32 v113, v126, v127
	v_cvt_pk_bf16_f32 v114, v120, v121
	v_cvt_pk_bf16_f32 v115, v122, v123
	v_cvt_pk_bf16_f32 v116, v116, v117
	v_cvt_pk_bf16_f32 v117, v118, v119
	v_cvt_pk_bf16_f32 v118, v140, v141
	v_cvt_pk_bf16_f32 v119, v130, v131
	global_store_dwordx4 v[128:129], v[112:115], off
	global_store_dwordx4 v[128:129], v[116:119], off offset:256
	s_nop 0
	v_or_b32_e32 v112, 16, v134
	v_cndmask_b32_e64 v113, 0, 1, s[40:41]
	v_cmp_ne_u32_e64 s[4:5], 1, v113
	s_andn2_b64 vcc, exec, s[40:41]
	v_ashrrev_i32_e32 v113, 31, v112
	s_cbranch_vccnz .LBB0_1681
; #define GAS __attribute__((address_space(1)))
;     __device__ __forceinline__ void operator()(const f32x4 (&acc)[2][2][4][2], const Unit& u, int wr, int wc, int fr, int fq) const {
;     ...
;                 const int row = row0 + ai * HALF + m * 16; bf16_t* rowp = base + (size_t)row * ld + col0;
;                 f32x4 v00 = acc[ai][0][m][0], v01 = acc[ai][0][m][1], v10 = acc[ai][1][m][0], v11 = acc[ai][1][m][1];
;                 if (do_rope) {
;                     const GAS u32x4* rp = (const GAS u32x4*)(rope + (size_t)row * 128 + wc * 32 + 8 * fq);
;                     const u32x4 ta = rp[0], tb = rp[1];
;                     { f32x4 a, b;
;                       a[0] = v00[0] * bf_lo(ta.x) - v10[0] * bf_hi(ta.x); b[0] = v10[0] * bf_lo(ta.x) + v00[0] * bf_hi(ta.x);
;                       a[1] = v00[1] * bf_lo(ta.y) - v10[1] * bf_hi(ta.y); b[1] = v10[1] * bf_lo(ta.y) + v00[1] * bf_hi(ta.y);
;                       a[2] = v00[2] * bf_lo(ta.z) - v10[2] * bf_hi(ta.z); b[2] = v10[2] * bf_lo(ta.z) + v00[2] * bf_hi(ta.z);
;                       a[3] = v00[3] * bf_lo(ta.w) - v10[3] * bf_hi(ta.w); b[3] = v10[3] * bf_lo(ta.w) + v00[3] * bf_hi(ta.w);
;                       v00 = a; v10 = b; }
;                     FENCE();
;                     { f32x4 a, b;
;                       a[0] = v01[0] * bf_lo(tb.x) - v11[0] * bf_hi(tb.x); b[0] = v11[0] * bf_lo(tb.x) + v01[0] * bf_hi(tb.x);
;                       a[1] = v01[1] * bf_lo(tb.y) - v11[1] * bf_hi(tb.y); b[1] = v11[1] * bf_lo(tb.y) + v01[1] * bf_hi(tb.y);
;                       a[2] = v01[2] * bf_lo(tb.z) - v11[2] * bf_hi(tb.z); b[2] = v11[2] * bf_lo(tb.z) + v01[2] * bf_hi(tb.z);
;                       a[3] = v01[3] * bf_lo(tb.w) - v11[3] * bf_hi(tb.w); b[3] = v11[3] * bf_lo(tb.w) + v01[3] * bf_hi(tb.w);
;                       v01 = a; v11 = b; }
;                 }
;                 v00 = v00 * sc; v01 = v01 * sc; v10 = v10 * sc; v11 = v11 * sc;
;                 u32x4 w0, w1;
;                 w0.x = cvt_pk_bf16(v00[0], v00[1]); w0.y = cvt_pk_bf16(v00[2], v00[3]); w0.z = cvt_pk_bf16(v01[0], v01[1]); w0.w = cvt_pk_bf16(v01[2], v01[3]);
;                 w1.x = cvt_pk_bf16(v10[0], v10[1]); w1.y = cvt_pk_bf16(v10[2], v10[3]); w1.z = cvt_pk_bf16(v11[0], v11[1]); w1.w = cvt_pk_bf16(v11[2], v11[3]);
;                 *(u32x4*)(rowp) = w0; *(u32x4*)(rowp + HALF) = w1;
	v_lshlrev_b64 v[114:115], 9, v[112:113]
	v_lshl_add_u64 v[114:115], s[20:21], 0, v[114:115]
	v_lshl_add_u64 v[118:119], v[114:115], 0, v[132:133]
	v_mov_b32_e32 v114, v166
	v_mov_b32_e32 v115, v167
	v_mov_b32_e32 v116, v168
	v_mov_b32_e32 v117, v169
	v_mov_b32_e32 v118, v170
	v_mov_b32_e32 v119, v171
	v_mov_b32_e32 v120, v172
	v_mov_b32_e32 v121, v173
	v_lshlrev_b32_e32 v113, 16, v116
	v_and_b32_e32 v127, 0xffff0000, v116
	v_lshlrev_b32_e32 v116, 16, v117
	v_and_b32_e32 v117, 0xffff0000, v117
	v_mul_f32_e32 v126, v110, v113
	v_mul_f32_e32 v128, v102, v127
	v_mul_f32_e32 v130, v102, v113
	v_mul_f32_e32 v140, v110, v127
	v_mov_b32_e32 v102, v111
	v_mov_b32_e32 v110, v103
	v_lshlrev_b32_e32 v123, 16, v115
	v_lshlrev_b32_e32 v122, 16, v114
	v_and_b32_e32 v115, 0xffff0000, v115
	v_and_b32_e32 v114, 0xffff0000, v114
	v_pk_mul_f32 v[102:103], v[102:103], v[116:117]
	v_pk_mul_f32 v[110:111], v[110:111], v[116:117]
	v_pk_mul_f32 v[124:125], v[108:109], v[114:115]
	v_pk_mul_f32 v[114:115], v[100:101], v[114:115]
	v_mov_b32_e32 v127, v102
	v_mov_b32_e32 v129, v103
	v_mov_b32_e32 v131, v110
	v_mov_b32_e32 v141, v111
	v_pk_fma_f32 v[108:109], v[108:109], v[122:123], v[114:115] neg_lo:[0,0,1] neg_hi:[0,0,1]
	v_pk_fma_f32 v[100:101], v[100:101], v[122:123], v[124:125]
	v_pk_add_f32 v[110:111], v[126:127], v[128:129] neg_lo:[0,1] neg_hi:[0,1]
	v_pk_add_f32 v[102:103], v[130:131], v[140:141]
	v_lshlrev_b32_e32 v113, 16, v120
	v_and_b32_e32 v123, 0xffff0000, v120
	v_mul_f32_e32 v120, v98, v123
	v_mul_f32_e32 v124, v98, v113
	v_lshlrev_b32_e32 v128, 16, v121
	v_and_b32_e32 v129, 0xffff0000, v121
	v_mov_b32_e32 v98, v107
	v_and_b32_e32 v117, 0xffff0000, v119
	v_and_b32_e32 v116, 0xffff0000, v118
	v_mul_f32_e32 v122, v106, v113
	v_mul_f32_e32 v126, v106, v123
	v_pk_mul_f32 v[130:131], v[98:99], v[128:129]
	v_mov_b32_e32 v106, v99
	v_lshlrev_b32_e32 v115, 16, v119
	v_lshlrev_b32_e32 v114, 16, v118
	v_pk_mul_f32 v[118:119], v[104:105], v[116:117]
	v_pk_mul_f32 v[116:117], v[96:97], v[116:117]
	v_mov_b32_e32 v123, v130
	v_mov_b32_e32 v121, v131
	v_pk_mul_f32 v[98:99], v[106:107], v[128:129]
	v_pk_fma_f32 v[104:105], v[104:105], v[114:115], v[116:117] neg_lo:[0,0,1] neg_hi:[0,0,1]
	v_pk_add_f32 v[116:117], v[122:123], v[120:121] neg_lo:[0,1] neg_hi:[0,1]
	v_mov_b32_e32 v125, v98
	v_mov_b32_e32 v127, v99
	v_pk_fma_f32 v[96:97], v[96:97], v[114:115], v[118:119]
	v_pk_add_f32 v[98:99], v[124:125], v[126:127]
	v_mov_b32_e32 v106, v116
	v_mov_b32_e32 v107, v117
.LBB0_1681:
	v_mov_b32_e32 v137, v136
	v_mad_i64_i32 v[114:115], s[40:41], v112, s76, v[138:139]
	v_mov_b32_e32 v112, v136
	v_mov_b32_e32 v113, v136
	v_pk_mul_f32 v[110:111], v[112:113], v[110:111]
	v_pk_mul_f32 v[108:109], v[136:137], v[108:109]
	v_pk_mul_f32 v[106:107], v[112:113], v[106:107]
	v_pk_mul_f32 v[104:105], v[136:137], v[104:105]
	v_pk_mul_f32 v[102:103], v[112:113], v[102:103]
	v_pk_mul_f32 v[100:101], v[136:137], v[100:101]
	v_pk_mul_f32 v[116:117], v[112:113], v[98:99]
	v_pk_mul_f32 v[118:119], v[136:137], v[96:97]
	v_cvt_pk_bf16_f32 v96, v108, v109
	v_cvt_pk_bf16_f32 v97, v110, v111
	v_cvt_pk_bf16_f32 v98, v104, v105
	v_cvt_pk_bf16_f32 v99, v106, v107
	v_cvt_pk_bf16_f32 v100, v100, v101
	v_cvt_pk_bf16_f32 v101, v102, v103
	s_nop 0
	v_cvt_pk_bf16_f32 v102, v118, v119
	v_cvt_pk_bf16_f32 v103, v116, v117
	global_store_dwordx4 v[114:115], v[96:99], off
	global_store_dwordx4 v[114:115], v[100:103], off offset:256
	s_nop 0
	v_or_b32_e32 v96, 32, v134
	s_and_b64 vcc, exec, s[4:5]
	v_ashrrev_i32_e32 v97, 31, v96
	s_cbranch_vccnz .LBB0_1683
	v_lshlrev_b64 v[98:99], 9, v[96:97]
	v_lshl_add_u64 v[98:99], s[20:21], 0, v[98:99]
	v_lshl_add_u64 v[102:103], v[98:99], 0, v[132:133]
	v_mov_b32_e32 v98, v174
	v_mov_b32_e32 v99, v175
	v_mov_b32_e32 v100, v176
	v_mov_b32_e32 v101, v177
	v_mov_b32_e32 v102, v178
	v_mov_b32_e32 v103, v179
	v_mov_b32_e32 v104, v180
	v_mov_b32_e32 v105, v181
	v_lshlrev_b32_e32 v97, 16, v100
	v_and_b32_e32 v111, 0xffff0000, v100
	v_lshlrev_b32_e32 v100, 16, v101
	v_and_b32_e32 v101, 0xffff0000, v101
	v_mul_f32_e32 v110, v94, v97
	v_mul_f32_e32 v114, v86, v111
	v_mul_f32_e32 v116, v86, v97
	v_mul_f32_e32 v118, v94, v111
	v_mov_b32_e32 v86, v95
	v_mov_b32_e32 v94, v87
	v_lshlrev_b32_e32 v107, 16, v99
	v_lshlrev_b32_e32 v106, 16, v98
	v_and_b32_e32 v99, 0xffff0000, v99
	v_and_b32_e32 v98, 0xffff0000, v98
	v_pk_mul_f32 v[86:87], v[86:87], v[100:101]
	v_pk_mul_f32 v[94:95], v[94:95], v[100:101]
	v_pk_mul_f32 v[108:109], v[92:93], v[98:99]
	v_pk_mul_f32 v[98:99], v[84:85], v[98:99]
	v_mov_b32_e32 v111, v86
	v_mov_b32_e32 v115, v87
	v_mov_b32_e32 v117, v94
	v_mov_b32_e32 v119, v95
	v_pk_fma_f32 v[92:93], v[92:93], v[106:107], v[98:99] neg_lo:[0,0,1] neg_hi:[0,0,1]
	v_pk_fma_f32 v[84:85], v[84:85], v[106:107], v[108:109]
	v_pk_add_f32 v[94:95], v[110:111], v[114:115] neg_lo:[0,1] neg_hi:[0,1]
	v_pk_add_f32 v[86:87], v[116:117], v[118:119]
	v_lshlrev_b32_e32 v97, 16, v104
	v_and_b32_e32 v107, 0xffff0000, v104
	v_mul_f32_e32 v104, v82, v107
	v_mul_f32_e32 v108, v82, v97
	v_lshlrev_b32_e32 v114, 16, v105
	v_and_b32_e32 v115, 0xffff0000, v105
	v_mov_b32_e32 v82, v91
	v_and_b32_e32 v101, 0xffff0000, v103
	v_and_b32_e32 v100, 0xffff0000, v102
	v_mul_f32_e32 v106, v90, v97
	v_mul_f32_e32 v110, v90, v107
	v_pk_mul_f32 v[116:117], v[82:83], v[114:115]
	v_mov_b32_e32 v90, v83
	v_lshlrev_b32_e32 v99, 16, v103
	v_lshlrev_b32_e32 v98, 16, v102
	v_pk_mul_f32 v[102:103], v[88:89], v[100:101]
	v_pk_mul_f32 v[100:101], v[80:81], v[100:101]
	v_mov_b32_e32 v107, v116
	v_mov_b32_e32 v105, v117
	v_pk_mul_f32 v[82:83], v[90:91], v[114:115]
	v_pk_fma_f32 v[88:89], v[88:89], v[98:99], v[100:101] neg_lo:[0,0,1] neg_hi:[0,0,1]
	v_pk_add_f32 v[100:101], v[106:107], v[104:105] neg_lo:[0,1] neg_hi:[0,1]
	v_mov_b32_e32 v109, v82
	v_mov_b32_e32 v111, v83
	v_pk_fma_f32 v[80:81], v[80:81], v[98:99], v[102:103]
	v_pk_add_f32 v[82:83], v[108:109], v[110:111]
	v_mov_b32_e32 v90, v100
	v_mov_b32_e32 v91, v101
; #define GAS __attribute__((address_space(1)))
;     __device__ __forceinline__ void operator()(const f32x4 (&acc)[2][2][4][2], const Unit& u, int wr, int wc, int fr, int fq) const {
;     ...
;                 const int row = row0 + ai * HALF + m * 16; bf16_t* rowp = base + (size_t)row * ld + col0;
;                 f32x4 v00 = acc[ai][0][m][0], v01 = acc[ai][0][m][1], v10 = acc[ai][1][m][0], v11 = acc[ai][1][m][1];
;                 if (do_rope) {
;                     const GAS u32x4* rp = (const GAS u32x4*)(rope + (size_t)row * 128 + wc * 32 + 8 * fq);
;                     const u32x4 ta = rp[0], tb = rp[1];
;                     { f32x4 a, b;
;                       a[0] = v00[0] * bf_lo(ta.x) - v10[0] * bf_hi(ta.x); b[0] = v10[0] * bf_lo(ta.x) + v00[0] * bf_hi(ta.x);
;                       a[1] = v00[1] * bf_lo(ta.y) - v10[1] * bf_hi(ta.y); b[1] = v10[1] * bf_lo(ta.y) + v00[1] * bf_hi(ta.y);
;                       a[2] = v00[2] * bf_lo(ta.z) - v10[2] * bf_hi(ta.z); b[2] = v10[2] * bf_lo(ta.z) + v00[2] * bf_hi(ta.z);
;                       a[3] = v00[3] * bf_lo(ta.w) - v10[3] * bf_hi(ta.w); b[3] = v10[3] * bf_lo(ta.w) + v00[3] * bf_hi(ta.w);
;                       v00 = a; v10 = b; }
;                     FENCE();
;                     { f32x4 a, b;
;                       a[0] = v01[0] * bf_lo(tb.x) - v11[0] * bf_hi(tb.x); b[0] = v11[0] * bf_lo(tb.x) + v01[0] * bf_hi(tb.x);
;                       a[1] = v01[1] * bf_lo(tb.y) - v11[1] * bf_hi(tb.y); b[1] = v11[1] * bf_lo(tb.y) + v01[1] * bf_hi(tb.y);
;                       a[2] = v01[2] * bf_lo(tb.z) - v11[2] * bf_hi(tb.z); b[2] = v11[2] * bf_lo(tb.z) + v01[2] * bf_hi(tb.z);
;                       a[3] = v01[3] * bf_lo(tb.w) - v11[3] * bf_hi(tb.w); b[3] = v11[3] * bf_lo(tb.w) + v01[3] * bf_hi(tb.w);
;                       v01 = a; v11 = b; }
;                 }
;                 v00 = v00 * sc; v01 = v01 * sc; v10 = v10 * sc; v11 = v11 * sc;
;                 u32x4 w0, w1;
;                 w0.x = cvt_pk_bf16(v00[0], v00[1]); w0.y = cvt_pk_bf16(v00[2], v00[3]); w0.z = cvt_pk_bf16(v01[0], v01[1]); w0.w = cvt_pk_bf16(v01[2], v01[3]);
;                 w1.x = cvt_pk_bf16(v10[0], v10[1]); w1.y = cvt_pk_bf16(v10[2], v10[3]); w1.z = cvt_pk_bf16(v11[0], v11[1]); w1.w = cvt_pk_bf16(v11[2], v11[3]);
;                 *(u32x4*)(rowp) = w0; *(u32x4*)(rowp + HALF) = w1;
.LBB0_1683:
	v_mad_i64_i32 v[96:97], s[40:41], v96, s76, v[138:139]
	v_pk_mul_f32 v[94:95], v[112:113], v[94:95]
	v_pk_mul_f32 v[92:93], v[136:137], v[92:93]
	v_pk_mul_f32 v[90:91], v[112:113], v[90:91]
	v_pk_mul_f32 v[88:89], v[136:137], v[88:89]
	v_pk_mul_f32 v[86:87], v[112:113], v[86:87]
	v_pk_mul_f32 v[84:85], v[136:137], v[84:85]
	v_pk_mul_f32 v[98:99], v[112:113], v[82:83]
	v_pk_mul_f32 v[100:101], v[136:137], v[80:81]
	v_cvt_pk_bf16_f32 v80, v92, v93
	v_cvt_pk_bf16_f32 v81, v94, v95
	v_cvt_pk_bf16_f32 v82, v88, v89
	v_cvt_pk_bf16_f32 v83, v90, v91
	v_cvt_pk_bf16_f32 v84, v84, v85
	v_cvt_pk_bf16_f32 v85, v86, v87
	s_nop 0
	v_cvt_pk_bf16_f32 v86, v100, v101
	v_cvt_pk_bf16_f32 v87, v98, v99
	global_store_dwordx4 v[96:97], v[80:83], off
	global_store_dwordx4 v[96:97], v[84:87], off offset:256
	s_nop 0
	v_or_b32_e32 v80, 48, v134
	s_and_b64 vcc, exec, s[4:5]
	v_ashrrev_i32_e32 v81, 31, v80
	s_cbranch_vccnz .LBB0_1685
	v_lshlrev_b64 v[82:83], 9, v[80:81]
	v_lshl_add_u64 v[82:83], s[20:21], 0, v[82:83]
	v_lshl_add_u64 v[86:87], v[82:83], 0, v[132:133]
	v_mov_b32_e32 v82, v182
	v_mov_b32_e32 v83, v183
	v_mov_b32_e32 v84, v184
	v_mov_b32_e32 v85, v185
	v_mov_b32_e32 v86, v186
	v_mov_b32_e32 v87, v187
	v_mov_b32_e32 v88, v188
	v_mov_b32_e32 v89, v189
	v_lshlrev_b32_e32 v81, 16, v84
	v_and_b32_e32 v95, 0xffff0000, v84
	v_lshlrev_b32_e32 v84, 16, v85
	v_and_b32_e32 v85, 0xffff0000, v85
	v_mul_f32_e32 v94, v78, v81
	v_mul_f32_e32 v96, v70, v95
	v_mul_f32_e32 v98, v70, v81
	v_mul_f32_e32 v100, v78, v95
	v_mov_b32_e32 v70, v79
	v_mov_b32_e32 v78, v71
	v_lshlrev_b32_e32 v91, 16, v83
	v_lshlrev_b32_e32 v90, 16, v82
	v_and_b32_e32 v83, 0xffff0000, v83
	v_and_b32_e32 v82, 0xffff0000, v82
	v_pk_mul_f32 v[70:71], v[70:71], v[84:85]
	v_pk_mul_f32 v[78:79], v[78:79], v[84:85]
	v_pk_mul_f32 v[92:93], v[76:77], v[82:83]
	v_pk_mul_f32 v[82:83], v[68:69], v[82:83]
	v_mov_b32_e32 v95, v70
	v_mov_b32_e32 v97, v71
	v_mov_b32_e32 v99, v78
	v_mov_b32_e32 v101, v79
	v_pk_fma_f32 v[76:77], v[76:77], v[90:91], v[82:83] neg_lo:[0,0,1] neg_hi:[0,0,1]
	v_pk_fma_f32 v[68:69], v[68:69], v[90:91], v[92:93]
	v_pk_add_f32 v[78:79], v[94:95], v[96:97] neg_lo:[0,1] neg_hi:[0,1]
	v_pk_add_f32 v[70:71], v[98:99], v[100:101]
	v_lshlrev_b32_e32 v81, 16, v88
	v_and_b32_e32 v91, 0xffff0000, v88
	v_mul_f32_e32 v88, v66, v91
	v_mul_f32_e32 v92, v66, v81
	v_lshlrev_b32_e32 v96, 16, v89
	v_and_b32_e32 v97, 0xffff0000, v89
	v_mov_b32_e32 v66, v75
	v_and_b32_e32 v85, 0xffff0000, v87
	v_and_b32_e32 v84, 0xffff0000, v86
	v_mul_f32_e32 v90, v74, v81
	v_mul_f32_e32 v94, v74, v91
	v_pk_mul_f32 v[98:99], v[66:67], v[96:97]
	v_mov_b32_e32 v74, v67
	v_lshlrev_b32_e32 v83, 16, v87
	v_lshlrev_b32_e32 v82, 16, v86
	v_pk_mul_f32 v[86:87], v[72:73], v[84:85]
	v_pk_mul_f32 v[84:85], v[64:65], v[84:85]
	v_mov_b32_e32 v91, v98
	v_mov_b32_e32 v89, v99
	v_pk_mul_f32 v[66:67], v[74:75], v[96:97]
	v_pk_fma_f32 v[72:73], v[72:73], v[82:83], v[84:85] neg_lo:[0,0,1] neg_hi:[0,0,1]
	v_pk_add_f32 v[84:85], v[90:91], v[88:89] neg_lo:[0,1] neg_hi:[0,1]
	v_mov_b32_e32 v93, v66
	v_mov_b32_e32 v95, v67
	v_pk_fma_f32 v[64:65], v[64:65], v[82:83], v[86:87]
	v_pk_add_f32 v[66:67], v[92:93], v[94:95]
	v_mov_b32_e32 v74, v84
	v_mov_b32_e32 v75, v85
.LBB0_1685:
	v_mad_i64_i32 v[82:83], s[40:41], v80, s76, v[138:139]
	v_mov_b32_e32 v80, v136
	v_mov_b32_e32 v81, v136
	v_pk_mul_f32 v[78:79], v[80:81], v[78:79]
	v_pk_mul_f32 v[76:77], v[136:137], v[76:77]
	v_pk_mul_f32 v[74:75], v[80:81], v[74:75]
	v_pk_mul_f32 v[72:73], v[136:137], v[72:73]
	v_pk_mul_f32 v[70:71], v[80:81], v[70:71]
	v_pk_mul_f32 v[68:69], v[136:137], v[68:69]
	v_pk_mul_f32 v[84:85], v[80:81], v[66:67]
	v_pk_mul_f32 v[86:87], v[136:137], v[64:65]
	v_cvt_pk_bf16_f32 v64, v76, v77
	v_cvt_pk_bf16_f32 v65, v78, v79
	v_cvt_pk_bf16_f32 v66, v72, v73
	v_cvt_pk_bf16_f32 v67, v74, v75
	v_cvt_pk_bf16_f32 v68, v68, v69
	v_cvt_pk_bf16_f32 v69, v70, v71
	s_nop 0
	v_cvt_pk_bf16_f32 v70, v86, v87
	v_cvt_pk_bf16_f32 v71, v84, v85
	global_store_dwordx4 v[82:83], v[64:67], off
	global_store_dwordx4 v[82:83], v[68:71], off offset:256
	s_nop 0
	v_add_u32_e32 v64, 0x80, v134
	s_and_b64 vcc, exec, s[4:5]
	v_ashrrev_i32_e32 v65, 31, v64
	s_cbranch_vccnz .LBB0_1687
	v_lshlrev_b64 v[66:67], 9, v[64:65]
	v_lshl_add_u64 v[66:67], s[20:21], 0, v[66:67]
	v_lshl_add_u64 v[70:71], v[66:67], 0, v[132:133]
	v_mov_b32_e32 v66, v190
	v_mov_b32_e32 v67, v191
	v_mov_b32_e32 v68, v192
	v_mov_b32_e32 v69, v193
	v_mov_b32_e32 v70, v194
	v_mov_b32_e32 v71, v195
	v_mov_b32_e32 v72, v196
	v_mov_b32_e32 v73, v197
	v_lshlrev_b32_e32 v65, 16, v68
	v_and_b32_e32 v79, 0xffff0000, v68
	v_lshlrev_b32_e32 v68, 16, v69
	v_and_b32_e32 v69, 0xffff0000, v69
	v_mul_f32_e32 v78, v62, v65
	v_mul_f32_e32 v82, v54, v79
	v_mul_f32_e32 v84, v54, v65
	v_mul_f32_e32 v86, v62, v79
	v_mov_b32_e32 v54, v63
	v_mov_b32_e32 v62, v55
	v_lshlrev_b32_e32 v75, 16, v67
	v_lshlrev_b32_e32 v74, 16, v66
	v_and_b32_e32 v67, 0xffff0000, v67
	v_and_b32_e32 v66, 0xffff0000, v66
	v_pk_mul_f32 v[54:55], v[54:55], v[68:69]
	v_pk_mul_f32 v[62:63], v[62:63], v[68:69]
	v_pk_mul_f32 v[76:77], v[60:61], v[66:67]
	v_pk_mul_f32 v[66:67], v[52:53], v[66:67]
	v_mov_b32_e32 v79, v54
	v_mov_b32_e32 v83, v55
	v_mov_b32_e32 v85, v62
	v_mov_b32_e32 v87, v63
	v_pk_fma_f32 v[60:61], v[60:61], v[74:75], v[66:67] neg_lo:[0,0,1] neg_hi:[0,0,1]
	v_pk_fma_f32 v[52:53], v[52:53], v[74:75], v[76:77]
	v_pk_add_f32 v[62:63], v[78:79], v[82:83] neg_lo:[0,1] neg_hi:[0,1]
	v_pk_add_f32 v[54:55], v[84:85], v[86:87]
	v_lshlrev_b32_e32 v65, 16, v72
	v_and_b32_e32 v75, 0xffff0000, v72
	v_mul_f32_e32 v72, v50, v75
	v_mul_f32_e32 v76, v50, v65
	v_lshlrev_b32_e32 v82, 16, v73
	v_and_b32_e32 v83, 0xffff0000, v73
	v_mov_b32_e32 v50, v59
	v_and_b32_e32 v69, 0xffff0000, v71
	v_and_b32_e32 v68, 0xffff0000, v70
	v_mul_f32_e32 v74, v58, v65
	v_mul_f32_e32 v78, v58, v75
	v_pk_mul_f32 v[84:85], v[50:51], v[82:83]
	v_mov_b32_e32 v58, v51
	v_lshlrev_b32_e32 v67, 16, v71
	v_lshlrev_b32_e32 v66, 16, v70
	v_pk_mul_f32 v[70:71], v[56:57], v[68:69]
	v_pk_mul_f32 v[68:69], v[48:49], v[68:69]
	v_mov_b32_e32 v75, v84
	v_mov_b32_e32 v73, v85
	v_pk_mul_f32 v[50:51], v[58:59], v[82:83]
	v_pk_fma_f32 v[56:57], v[56:57], v[66:67], v[68:69] neg_lo:[0,0,1] neg_hi:[0,0,1]
	v_pk_add_f32 v[68:69], v[74:75], v[72:73] neg_lo:[0,1] neg_hi:[0,1]
	v_mov_b32_e32 v77, v50
	v_mov_b32_e32 v79, v51
	v_pk_fma_f32 v[48:49], v[48:49], v[66:67], v[70:71]
	v_pk_add_f32 v[50:51], v[76:77], v[78:79]
	v_mov_b32_e32 v58, v68
	v_mov_b32_e32 v59, v69
; #define GAS __attribute__((address_space(1)))
;     __device__ __forceinline__ void operator()(const f32x4 (&acc)[2][2][4][2], const Unit& u, int wr, int wc, int fr, int fq) const {
;     ...
;                 const int row = row0 + ai * HALF + m * 16; bf16_t* rowp = base + (size_t)row * ld + col0;
;                 f32x4 v00 = acc[ai][0][m][0], v01 = acc[ai][0][m][1], v10 = acc[ai][1][m][0], v11 = acc[ai][1][m][1];
;                 if (do_rope) {
;                     const GAS u32x4* rp = (const GAS u32x4*)(rope + (size_t)row * 128 + wc * 32 + 8 * fq);
;                     const u32x4 ta = rp[0], tb = rp[1];
;                     { f32x4 a, b;
;                       a[0] = v00[0] * bf_lo(ta.x) - v10[0] * bf_hi(ta.x); b[0] = v10[0] * bf_lo(ta.x) + v00[0] * bf_hi(ta.x);
;                       a[1] = v00[1] * bf_lo(ta.y) - v10[1] * bf_hi(ta.y); b[1] = v10[1] * bf_lo(ta.y) + v00[1] * bf_hi(ta.y);
;                       a[2] = v00[2] * bf_lo(ta.z) - v10[2] * bf_hi(ta.z); b[2] = v10[2] * bf_lo(ta.z) + v00[2] * bf_hi(ta.z);
;                       a[3] = v00[3] * bf_lo(ta.w) - v10[3] * bf_hi(ta.w); b[3] = v10[3] * bf_lo(ta.w) + v00[3] * bf_hi(ta.w);
;                       v00 = a; v10 = b; }
;                     FENCE();
;                     { f32x4 a, b;
;                       a[0] = v01[0] * bf_lo(tb.x) - v11[0] * bf_hi(tb.x); b[0] = v11[0] * bf_lo(tb.x) + v01[0] * bf_hi(tb.x);
;                       a[1] = v01[1] * bf_lo(tb.y) - v11[1] * bf_hi(tb.y); b[1] = v11[1] * bf_lo(tb.y) + v01[1] * bf_hi(tb.y);
;                       a[2] = v01[2] * bf_lo(tb.z) - v11[2] * bf_hi(tb.z); b[2] = v11[2] * bf_lo(tb.z) + v01[2] * bf_hi(tb.z);
;                       a[3] = v01[3] * bf_lo(tb.w) - v11[3] * bf_hi(tb.w); b[3] = v11[3] * bf_lo(tb.w) + v01[3] * bf_hi(tb.w);
;                       v01 = a; v11 = b; }
;                 }
;                 v00 = v00 * sc; v01 = v01 * sc; v10 = v10 * sc; v11 = v11 * sc;
;                 u32x4 w0, w1;
;                 w0.x = cvt_pk_bf16(v00[0], v00[1]); w0.y = cvt_pk_bf16(v00[2], v00[3]); w0.z = cvt_pk_bf16(v01[0], v01[1]); w0.w = cvt_pk_bf16(v01[2], v01[3]);
;                 w1.x = cvt_pk_bf16(v10[0], v10[1]); w1.y = cvt_pk_bf16(v10[2], v10[3]); w1.z = cvt_pk_bf16(v11[0], v11[1]); w1.w = cvt_pk_bf16(v11[2], v11[3]);
;                 *(u32x4*)(rowp) = w0; *(u32x4*)(rowp + HALF) = w1;
.LBB0_1687:
	v_mad_i64_i32 v[64:65], s[40:41], v64, s76, v[138:139]
	v_pk_mul_f32 v[62:63], v[80:81], v[62:63]
	v_pk_mul_f32 v[60:61], v[136:137], v[60:61]
	v_pk_mul_f32 v[58:59], v[80:81], v[58:59]
	v_pk_mul_f32 v[56:57], v[136:137], v[56:57]
	v_pk_mul_f32 v[54:55], v[80:81], v[54:55]
	v_pk_mul_f32 v[52:53], v[136:137], v[52:53]
	v_pk_mul_f32 v[66:67], v[80:81], v[50:51]
	v_pk_mul_f32 v[68:69], v[136:137], v[48:49]
	v_cvt_pk_bf16_f32 v48, v60, v61
	v_cvt_pk_bf16_f32 v49, v62, v63
	v_cvt_pk_bf16_f32 v50, v56, v57
	v_cvt_pk_bf16_f32 v51, v58, v59
	v_cvt_pk_bf16_f32 v52, v52, v53
	v_cvt_pk_bf16_f32 v53, v54, v55
	s_nop 0
	v_cvt_pk_bf16_f32 v54, v68, v69
	v_cvt_pk_bf16_f32 v55, v66, v67
	global_store_dwordx4 v[64:65], v[48:51], off
	global_store_dwordx4 v[64:65], v[52:55], off offset:256
	s_nop 0
	v_add_u32_e32 v48, 0x90, v134
	s_and_b64 vcc, exec, s[4:5]
	v_ashrrev_i32_e32 v49, 31, v48
	s_cbranch_vccnz .LBB0_1689
	v_lshlrev_b64 v[50:51], 9, v[48:49]
	v_lshl_add_u64 v[50:51], s[20:21], 0, v[50:51]
	v_lshl_add_u64 v[54:55], v[50:51], 0, v[132:133]
	v_mov_b32_e32 v50, v198
	v_mov_b32_e32 v51, v199
	v_mov_b32_e32 v52, v200
	v_mov_b32_e32 v53, v201
	v_mov_b32_e32 v54, v202
	v_mov_b32_e32 v55, v203
	v_mov_b32_e32 v56, v204
	v_mov_b32_e32 v57, v205
	v_lshlrev_b32_e32 v49, 16, v52
	v_and_b32_e32 v63, 0xffff0000, v52
	v_lshlrev_b32_e32 v52, 16, v53
	v_and_b32_e32 v53, 0xffff0000, v53
	v_mul_f32_e32 v62, v46, v49
	v_mul_f32_e32 v64, v38, v63
	v_mul_f32_e32 v66, v38, v49
	v_mul_f32_e32 v68, v46, v63
	v_mov_b32_e32 v38, v47
	v_mov_b32_e32 v46, v39
	v_lshlrev_b32_e32 v59, 16, v51
	v_lshlrev_b32_e32 v58, 16, v50
	v_and_b32_e32 v51, 0xffff0000, v51
	v_and_b32_e32 v50, 0xffff0000, v50
	v_pk_mul_f32 v[38:39], v[38:39], v[52:53]
	v_pk_mul_f32 v[46:47], v[46:47], v[52:53]
	v_pk_mul_f32 v[60:61], v[44:45], v[50:51]
	v_pk_mul_f32 v[50:51], v[36:37], v[50:51]
	v_mov_b32_e32 v63, v38
	v_mov_b32_e32 v65, v39
	v_mov_b32_e32 v67, v46
	v_mov_b32_e32 v69, v47
	v_pk_fma_f32 v[44:45], v[44:45], v[58:59], v[50:51] neg_lo:[0,0,1] neg_hi:[0,0,1]
	v_pk_fma_f32 v[36:37], v[36:37], v[58:59], v[60:61]
	v_pk_add_f32 v[46:47], v[62:63], v[64:65] neg_lo:[0,1] neg_hi:[0,1]
	v_pk_add_f32 v[38:39], v[66:67], v[68:69]
	v_lshlrev_b32_e32 v49, 16, v56
	v_and_b32_e32 v59, 0xffff0000, v56
	v_mul_f32_e32 v56, v34, v59
	v_mul_f32_e32 v60, v34, v49
	v_lshlrev_b32_e32 v64, 16, v57
	v_and_b32_e32 v65, 0xffff0000, v57
	v_mov_b32_e32 v34, v43
	v_and_b32_e32 v53, 0xffff0000, v55
	v_and_b32_e32 v52, 0xffff0000, v54
	v_mul_f32_e32 v58, v42, v49
	v_mul_f32_e32 v62, v42, v59
	v_pk_mul_f32 v[66:67], v[34:35], v[64:65]
	v_mov_b32_e32 v42, v35
	v_lshlrev_b32_e32 v51, 16, v55
	v_lshlrev_b32_e32 v50, 16, v54
	v_pk_mul_f32 v[54:55], v[40:41], v[52:53]
	v_pk_mul_f32 v[52:53], v[32:33], v[52:53]
	v_mov_b32_e32 v59, v66
	v_mov_b32_e32 v57, v67
	v_pk_mul_f32 v[34:35], v[42:43], v[64:65]
	v_pk_fma_f32 v[40:41], v[40:41], v[50:51], v[52:53] neg_lo:[0,0,1] neg_hi:[0,0,1]
	v_pk_add_f32 v[52:53], v[58:59], v[56:57] neg_lo:[0,1] neg_hi:[0,1]
	v_mov_b32_e32 v61, v34
	v_mov_b32_e32 v63, v35
	v_pk_fma_f32 v[32:33], v[32:33], v[50:51], v[54:55]
	v_pk_add_f32 v[34:35], v[60:61], v[62:63]
	v_mov_b32_e32 v42, v52
	v_mov_b32_e32 v43, v53
; #define GAS __attribute__((address_space(1)))
;     __device__ __forceinline__ void operator()(const f32x4 (&acc)[2][2][4][2], const Unit& u, int wr, int wc, int fr, int fq) const {
;     ...
;                 const int row = row0 + ai * HALF + m * 16; bf16_t* rowp = base + (size_t)row * ld + col0;
;                 f32x4 v00 = acc[ai][0][m][0], v01 = acc[ai][0][m][1], v10 = acc[ai][1][m][0], v11 = acc[ai][1][m][1];
;                 if (do_rope) {
;                     const GAS u32x4* rp = (const GAS u32x4*)(rope + (size_t)row * 128 + wc * 32 + 8 * fq);
;                     const u32x4 ta = rp[0], tb = rp[1];
;                     { f32x4 a, b;
;                       a[0] = v00[0] * bf_lo(ta.x) - v10[0] * bf_hi(ta.x); b[0] = v10[0] * bf_lo(ta.x) + v00[0] * bf_hi(ta.x);
;                       a[1] = v00[1] * bf_lo(ta.y) - v10[1] * bf_hi(ta.y); b[1] = v10[1] * bf_lo(ta.y) + v00[1] * bf_hi(ta.y);
;                       a[2] = v00[2] * bf_lo(ta.z) - v10[2] * bf_hi(ta.z); b[2] = v10[2] * bf_lo(ta.z) + v00[2] * bf_hi(ta.z);
;                       a[3] = v00[3] * bf_lo(ta.w) - v10[3] * bf_hi(ta.w); b[3] = v10[3] * bf_lo(ta.w) + v00[3] * bf_hi(ta.w);
;                       v00 = a; v10 = b; }
;                     FENCE();
;                     { f32x4 a, b;
;                       a[0] = v01[0] * bf_lo(tb.x) - v11[0] * bf_hi(tb.x); b[0] = v11[0] * bf_lo(tb.x) + v01[0] * bf_hi(tb.x);
;                       a[1] = v01[1] * bf_lo(tb.y) - v11[1] * bf_hi(tb.y); b[1] = v11[1] * bf_lo(tb.y) + v01[1] * bf_hi(tb.y);
;                       a[2] = v01[2] * bf_lo(tb.z) - v11[2] * bf_hi(tb.z); b[2] = v11[2] * bf_lo(tb.z) + v01[2] * bf_hi(tb.z);
;                       a[3] = v01[3] * bf_lo(tb.w) - v11[3] * bf_hi(tb.w); b[3] = v11[3] * bf_lo(tb.w) + v01[3] * bf_hi(tb.w);
;                       v01 = a; v11 = b; }
;                 }
;                 v00 = v00 * sc; v01 = v01 * sc; v10 = v10 * sc; v11 = v11 * sc;
;                 u32x4 w0, w1;
;                 w0.x = cvt_pk_bf16(v00[0], v00[1]); w0.y = cvt_pk_bf16(v00[2], v00[3]); w0.z = cvt_pk_bf16(v01[0], v01[1]); w0.w = cvt_pk_bf16(v01[2], v01[3]);
;                 w1.x = cvt_pk_bf16(v10[0], v10[1]); w1.y = cvt_pk_bf16(v10[2], v10[3]); w1.z = cvt_pk_bf16(v11[0], v11[1]); w1.w = cvt_pk_bf16(v11[2], v11[3]);
;                 *(u32x4*)(rowp) = w0; *(u32x4*)(rowp + HALF) = w1;
.LBB0_1689:
	v_mad_i64_i32 v[50:51], s[40:41], v48, s76, v[138:139]
	v_mov_b32_e32 v48, v136
	v_mov_b32_e32 v49, v136
	v_pk_mul_f32 v[46:47], v[48:49], v[46:47]
	v_pk_mul_f32 v[44:45], v[136:137], v[44:45]
	v_pk_mul_f32 v[42:43], v[48:49], v[42:43]
	v_pk_mul_f32 v[40:41], v[136:137], v[40:41]
	v_pk_mul_f32 v[38:39], v[48:49], v[38:39]
	v_pk_mul_f32 v[36:37], v[136:137], v[36:37]
	v_pk_mul_f32 v[52:53], v[48:49], v[34:35]
	v_pk_mul_f32 v[54:55], v[136:137], v[32:33]
	v_cvt_pk_bf16_f32 v32, v44, v45
	v_cvt_pk_bf16_f32 v33, v46, v47
	v_cvt_pk_bf16_f32 v34, v40, v41
	v_cvt_pk_bf16_f32 v35, v42, v43
	v_cvt_pk_bf16_f32 v36, v36, v37
	v_cvt_pk_bf16_f32 v37, v38, v39
	s_nop 0
	v_cvt_pk_bf16_f32 v38, v54, v55
	v_cvt_pk_bf16_f32 v39, v52, v53
	global_store_dwordx4 v[50:51], v[32:35], off
	global_store_dwordx4 v[50:51], v[36:39], off offset:256
	s_nop 0
	v_add_u32_e32 v32, 0xa0, v134
	s_and_b64 vcc, exec, s[4:5]
	v_ashrrev_i32_e32 v33, 31, v32
	s_cbranch_vccnz .LBB0_1691
	v_lshlrev_b64 v[34:35], 9, v[32:33]
	v_lshl_add_u64 v[34:35], s[20:21], 0, v[34:35]
	v_lshl_add_u64 v[38:39], v[34:35], 0, v[132:133]
	v_mov_b32_e32 v34, v206
	v_mov_b32_e32 v35, v207
	v_mov_b32_e32 v36, v208
	v_mov_b32_e32 v37, v209
	v_mov_b32_e32 v38, v210
	v_mov_b32_e32 v39, v211
	v_mov_b32_e32 v40, v212
	v_mov_b32_e32 v41, v213
	v_lshlrev_b32_e32 v33, 16, v36
	v_and_b32_e32 v47, 0xffff0000, v36
	v_lshlrev_b32_e32 v36, 16, v37
	v_and_b32_e32 v37, 0xffff0000, v37
	v_mul_f32_e32 v46, v30, v33
	v_mul_f32_e32 v50, v22, v47
	v_mul_f32_e32 v52, v22, v33
	v_mul_f32_e32 v54, v30, v47
	v_mov_b32_e32 v22, v31
	v_mov_b32_e32 v30, v23
	v_lshlrev_b32_e32 v43, 16, v35
	v_lshlrev_b32_e32 v42, 16, v34
	v_and_b32_e32 v35, 0xffff0000, v35
	v_and_b32_e32 v34, 0xffff0000, v34
	v_pk_mul_f32 v[22:23], v[22:23], v[36:37]
	v_pk_mul_f32 v[30:31], v[30:31], v[36:37]
	v_pk_mul_f32 v[44:45], v[28:29], v[34:35]
	v_pk_mul_f32 v[34:35], v[20:21], v[34:35]
	v_mov_b32_e32 v47, v22
	v_mov_b32_e32 v51, v23
	v_mov_b32_e32 v53, v30
	v_mov_b32_e32 v55, v31
	v_pk_fma_f32 v[28:29], v[28:29], v[42:43], v[34:35] neg_lo:[0,0,1] neg_hi:[0,0,1]
	v_pk_fma_f32 v[20:21], v[20:21], v[42:43], v[44:45]
	v_pk_add_f32 v[30:31], v[46:47], v[50:51] neg_lo:[0,1] neg_hi:[0,1]
	v_pk_add_f32 v[22:23], v[52:53], v[54:55]
	v_lshlrev_b32_e32 v33, 16, v40
	v_and_b32_e32 v43, 0xffff0000, v40
	v_mul_f32_e32 v40, v18, v43
	v_mul_f32_e32 v44, v18, v33
	v_lshlrev_b32_e32 v50, 16, v41
	v_and_b32_e32 v51, 0xffff0000, v41
	v_mov_b32_e32 v18, v27
	v_and_b32_e32 v37, 0xffff0000, v39
	v_and_b32_e32 v36, 0xffff0000, v38
	v_mul_f32_e32 v42, v26, v33
	v_mul_f32_e32 v46, v26, v43
	v_pk_mul_f32 v[52:53], v[18:19], v[50:51]
	v_mov_b32_e32 v26, v19
	v_lshlrev_b32_e32 v35, 16, v39
	v_lshlrev_b32_e32 v34, 16, v38
	v_pk_mul_f32 v[38:39], v[24:25], v[36:37]
	v_pk_mul_f32 v[36:37], v[16:17], v[36:37]
	v_mov_b32_e32 v43, v52
	v_mov_b32_e32 v41, v53
	v_pk_mul_f32 v[18:19], v[26:27], v[50:51]
	v_pk_fma_f32 v[24:25], v[24:25], v[34:35], v[36:37] neg_lo:[0,0,1] neg_hi:[0,0,1]
	v_pk_add_f32 v[36:37], v[42:43], v[40:41] neg_lo:[0,1] neg_hi:[0,1]
	v_mov_b32_e32 v45, v18
	v_mov_b32_e32 v47, v19
	v_pk_fma_f32 v[16:17], v[16:17], v[34:35], v[38:39]
	v_pk_add_f32 v[18:19], v[44:45], v[46:47]
	v_mov_b32_e32 v26, v36
	v_mov_b32_e32 v27, v37
.LBB0_1691:
	v_mad_i64_i32 v[32:33], s[40:41], v32, s76, v[138:139]
	v_pk_mul_f32 v[30:31], v[48:49], v[30:31]
	v_pk_mul_f32 v[28:29], v[136:137], v[28:29]
	v_pk_mul_f32 v[26:27], v[48:49], v[26:27]
	v_pk_mul_f32 v[24:25], v[136:137], v[24:25]
	v_pk_mul_f32 v[22:23], v[48:49], v[22:23]
	v_pk_mul_f32 v[20:21], v[136:137], v[20:21]
	v_pk_mul_f32 v[34:35], v[48:49], v[18:19]
	v_pk_mul_f32 v[36:37], v[136:137], v[16:17]
	v_cvt_pk_bf16_f32 v16, v28, v29
	v_cvt_pk_bf16_f32 v17, v30, v31
	v_cvt_pk_bf16_f32 v18, v24, v25
	v_cvt_pk_bf16_f32 v19, v26, v27
	v_cvt_pk_bf16_f32 v20, v20, v21
	v_cvt_pk_bf16_f32 v21, v22, v23
	s_nop 0
	v_cvt_pk_bf16_f32 v22, v36, v37
	v_cvt_pk_bf16_f32 v23, v34, v35
	global_store_dwordx4 v[32:33], v[16:19], off
	global_store_dwordx4 v[32:33], v[20:23], off offset:256
	s_nop 0
	v_add_u32_e32 v16, 0xb0, v134
	s_and_b64 vcc, exec, s[4:5]
	v_ashrrev_i32_e32 v17, 31, v16
	s_cbranch_vccnz .LBB0_1693
	v_lshlrev_b64 v[18:19], 9, v[16:17]
	v_lshl_add_u64 v[18:19], s[20:21], 0, v[18:19]
	v_lshl_add_u64 v[22:23], v[18:19], 0, v[132:133]
	v_mov_b32_e32 v18, v214
	v_mov_b32_e32 v19, v215
	v_mov_b32_e32 v20, v216
	v_mov_b32_e32 v21, v217
	v_mov_b32_e32 v22, v218
	v_mov_b32_e32 v23, v219
	v_mov_b32_e32 v24, v220
	v_mov_b32_e32 v25, v221
	v_lshlrev_b32_e32 v17, 16, v20
	v_and_b32_e32 v31, 0xffff0000, v20
	v_lshlrev_b32_e32 v20, 16, v21
	v_and_b32_e32 v21, 0xffff0000, v21
	v_mul_f32_e32 v30, v14, v17
	v_mul_f32_e32 v32, v6, v31
	v_mul_f32_e32 v34, v6, v17
	v_mul_f32_e32 v36, v14, v31
	v_mov_b32_e32 v6, v15
	v_mov_b32_e32 v14, v7
	v_lshlrev_b32_e32 v27, 16, v19
	v_lshlrev_b32_e32 v26, 16, v18
	v_and_b32_e32 v19, 0xffff0000, v19
	v_and_b32_e32 v18, 0xffff0000, v18
	v_pk_mul_f32 v[6:7], v[6:7], v[20:21]
	v_pk_mul_f32 v[14:15], v[14:15], v[20:21]
	v_pk_mul_f32 v[28:29], v[12:13], v[18:19]
	v_pk_mul_f32 v[18:19], v[4:5], v[18:19]
	v_mov_b32_e32 v31, v6
	v_mov_b32_e32 v33, v7
	v_mov_b32_e32 v35, v14
	v_mov_b32_e32 v37, v15
	v_pk_fma_f32 v[12:13], v[12:13], v[26:27], v[18:19] neg_lo:[0,0,1] neg_hi:[0,0,1]
	v_pk_fma_f32 v[4:5], v[4:5], v[26:27], v[28:29]
	v_pk_add_f32 v[14:15], v[30:31], v[32:33] neg_lo:[0,1] neg_hi:[0,1]
	v_pk_add_f32 v[6:7], v[34:35], v[36:37]
	v_lshlrev_b32_e32 v17, 16, v24
	v_and_b32_e32 v27, 0xffff0000, v24
	v_mul_f32_e32 v24, v2, v27
	v_mul_f32_e32 v28, v2, v17
	v_lshlrev_b32_e32 v32, 16, v25
	v_and_b32_e32 v33, 0xffff0000, v25
	v_mov_b32_e32 v2, v11
	v_and_b32_e32 v21, 0xffff0000, v23
	v_and_b32_e32 v20, 0xffff0000, v22
	v_mul_f32_e32 v26, v10, v17
	v_mul_f32_e32 v30, v10, v27
	v_pk_mul_f32 v[34:35], v[2:3], v[32:33]
	v_mov_b32_e32 v10, v3
	v_lshlrev_b32_e32 v19, 16, v23
	v_lshlrev_b32_e32 v18, 16, v22
	v_pk_mul_f32 v[22:23], v[8:9], v[20:21]
	v_pk_mul_f32 v[20:21], v[0:1], v[20:21]
	v_mov_b32_e32 v27, v34
	v_mov_b32_e32 v25, v35
	v_pk_mul_f32 v[2:3], v[10:11], v[32:33]
	v_pk_fma_f32 v[8:9], v[8:9], v[18:19], v[20:21] neg_lo:[0,0,1] neg_hi:[0,0,1]
	v_pk_add_f32 v[20:21], v[26:27], v[24:25] neg_lo:[0,1] neg_hi:[0,1]
	v_mov_b32_e32 v29, v2
	v_mov_b32_e32 v31, v3
	v_pk_fma_f32 v[0:1], v[0:1], v[18:19], v[22:23]
	v_pk_add_f32 v[2:3], v[28:29], v[30:31]
	v_mov_b32_e32 v10, v20
	v_mov_b32_e32 v11, v21
